# attention unit prologue: first K/V tile loads issued together with the Q loads (before the norm math and barrier), on top of v7_krope
# speedup vs baseline: 1.0095x; 1.0015x over previous
.LBB0_1115:
	v_add_u32_e32 v4, s3, v191
	v_ashrrev_i32_e32 v5, 31, v4
	s_and_saveexec_b64 s[0:1], s[38:39]
	s_xor_b64 s[0:1], exec, s[0:1]
	v_lshlrev_b64 v[4:5], 6, v[4:5]
	s_movk_i32 s24, 0xff80
	v_lshl_add_u64 v[4:5], v[182:183], 0, v[4:5]
	s_mov_b32 s25, -1
	v_lshl_add_u64 v[8:9], v[4:5], 0, s[24:25]
	s_or_saveexec_b64 s[0:1], s[0:1]
	s_and_b32 s35, s15, 7
	s_xor_b64 exec, exec, s[0:1]
	v_lshlrev_b64 v[4:5], 10, v[4:5]
	v_lshl_add_u64 v[4:5], s[48:49], 0, v[4:5]
	s_lshl_b32 s30, s35, 7
	v_lshl_add_u64 v[4:5], v[4:5], 0, s[30:31]
	v_lshl_add_u64 v[8:9], v[184:185], 1, v[4:5]
	s_or_b64 exec, exec, s[0:1]
	v_add_u32_e32 v4, s3, v193
	v_ashrrev_i32_e32 v5, 31, v4
	s_and_saveexec_b64 s[0:1], s[40:41]
	s_xor_b64 s[0:1], exec, s[0:1]
	v_lshlrev_b64 v[4:5], 6, v[4:5]
	s_movk_i32 s24, 0xff80
	v_lshl_add_u64 v[4:5], v[186:187], 0, v[4:5]
	s_mov_b32 s25, -1
	v_lshl_add_u64 v[10:11], v[4:5], 0, s[24:25]
	s_or_saveexec_b64 s[0:1], s[0:1]
	v_mov_b32_e32 v199, 0x1000
	s_xor_b64 exec, exec, s[0:1]
	v_lshlrev_b64 v[4:5], 10, v[4:5]
	v_lshl_add_u64 v[4:5], s[48:49], 0, v[4:5]
	s_lshl_b32 s30, s35, 7
	v_lshl_add_u64 v[4:5], v[4:5], 0, s[30:31]
	v_lshl_add_u64 v[10:11], v[188:189], 1, v[4:5]
	v_mov_b32_e32 v199, 0x10000
	s_or_b64 exec, exec, s[0:1]
	v_add_u32_e32 v200, s7, v214
	v_mov_b64_e32 v[4:5], s[46:47]
	s_movk_i32 s0, 0x600
	v_mad_i64_i32 v[4:5], s[0:1], v200, s0, v[4:5]
	s_mul_i32 s30, s35, 0xc0
	v_lshl_add_u64 v[4:5], v[4:5], 0, s[30:31]
	v_lshl_add_u64 v[4:5], v[4:5], 0, v[2:3]
	global_load_dwordx4 v[132:135], v[4:5], off
	global_load_dwordx4 v[136:139], v[4:5], off offset:32
	global_load_dwordx4 v[140:143], v[4:5], off offset:64
	global_load_dwordx4 v[144:147], v[4:5], off offset:96
	global_load_dwordx4 v[148:151], v[4:5], off offset:128
	global_load_dwordx4 v[152:155], v[4:5], off offset:160
	s_lshl_b32 s0, s2, 3
	s_or_b32 s0, s0, s35
	v_lshl_add_u32 v156, s0, 6, v203
	v_lshl_add_u32 v160, v190, 1, v10
	v_mad_u64_u32 v[158:159], vcc, v156, s28, v[192:193]
	v_subrev_u32_e32 v160, s44, v160
	v_subrev_u32_e32 v161, s44, v8
	s_or_b32 s0, s23, 1
	s_sub_i32 s1, s0, s34
	s_min_u32 s0, s0, s1
	v_mad_i32_i24 v162, v199, s23, v160
	v_lshl_add_u32 v163, s23, 7, v158
	v_lshl_add_u32 v164, s23, v215, v161
	v_lshl_add_u32 v165, s0, v215, v161
	v_mad_i32_i24 v156, v199, s0, v160
	global_load_dwordx2 v[120:121], v162, s[44:45]
	global_load_dwordx4 v[122:125], v163, s[44:45]
	global_load_dwordx4 v[116:119], v164, s[44:45]
	global_load_dwordx4 v[126:129], v165, s[44:45]
	global_load_dwordx2 v[130:131], v156, s[44:45]
	s_andn2_b64 vcc, exec, s[12:13]
	s_mov_b64 s[0:1], -1
	s_cbranch_vccnz .LBB0_1125
	s_mov_b64 s[0:1], 0

.LBB0_1127:
	s_lshl_b32 s0, s2, 3
	s_or_b32 s0, s0, s35
	v_lshl_add_u32 v5, s0, 6, v203
	v_lshl_add_u32 v4, v190, 1, v10
	v_mad_u64_u32 v[204:205], s[12:13], v5, s28, v[192:193]
	s_waitcnt vmcnt(0)
	v_and_b32_e32 v5, 0xffff0000, v132
	v_subrev_u32_e32 v202, s44, v4
	v_lshlrev_b32_e32 v4, 16, v132
	v_mul_f32_e32 v6, v5, v5
	v_fmac_f32_e32 v6, v4, v4
	v_lshlrev_b32_e32 v4, 16, v133
	v_fmac_f32_e32 v6, v4, v4
	v_and_b32_e32 v4, 0xffff0000, v133
	v_fmac_f32_e32 v6, v4, v4
	v_lshlrev_b32_e32 v4, 16, v134
	v_fmac_f32_e32 v6, v4, v4
	v_and_b32_e32 v4, 0xffff0000, v134
	v_fmac_f32_e32 v6, v4, v4
	v_lshlrev_b32_e32 v4, 16, v135
	v_fmac_f32_e32 v6, v4, v4
	v_and_b32_e32 v4, 0xffff0000, v135
	v_fmac_f32_e32 v6, v4, v4
	v_lshlrev_b32_e32 v4, 16, v136
	v_fmac_f32_e32 v6, v4, v4
	v_and_b32_e32 v4, 0xffff0000, v136
	v_fmac_f32_e32 v6, v4, v4
	v_lshlrev_b32_e32 v4, 16, v137
	v_fmac_f32_e32 v6, v4, v4
	v_and_b32_e32 v4, 0xffff0000, v137
	v_fmac_f32_e32 v6, v4, v4
	v_lshlrev_b32_e32 v4, 16, v138
	v_fmac_f32_e32 v6, v4, v4
	v_and_b32_e32 v4, 0xffff0000, v138
	v_fmac_f32_e32 v6, v4, v4
	v_lshlrev_b32_e32 v4, 16, v139
	v_fmac_f32_e32 v6, v4, v4
	v_and_b32_e32 v4, 0xffff0000, v139
	v_fmac_f32_e32 v6, v4, v4
	v_lshlrev_b32_e32 v4, 16, v140
	v_fmac_f32_e32 v6, v4, v4
	v_and_b32_e32 v4, 0xffff0000, v140
	v_fmac_f32_e32 v6, v4, v4
	v_lshlrev_b32_e32 v4, 16, v141
	v_fmac_f32_e32 v6, v4, v4
	v_and_b32_e32 v4, 0xffff0000, v141
	v_fmac_f32_e32 v6, v4, v4
	v_lshlrev_b32_e32 v4, 16, v142
	v_fmac_f32_e32 v6, v4, v4
	v_and_b32_e32 v4, 0xffff0000, v142
	v_fmac_f32_e32 v6, v4, v4
	v_lshlrev_b32_e32 v4, 16, v143
	v_fmac_f32_e32 v6, v4, v4
	v_and_b32_e32 v4, 0xffff0000, v143
	v_fmac_f32_e32 v6, v4, v4
	v_lshlrev_b32_e32 v4, 16, v144
	v_fmac_f32_e32 v6, v4, v4
	v_and_b32_e32 v4, 0xffff0000, v144
	v_fmac_f32_e32 v6, v4, v4
	v_lshlrev_b32_e32 v4, 16, v145
	v_fmac_f32_e32 v6, v4, v4
	v_and_b32_e32 v4, 0xffff0000, v145
	v_fmac_f32_e32 v6, v4, v4
	v_lshlrev_b32_e32 v4, 16, v146
	v_fmac_f32_e32 v6, v4, v4
	v_and_b32_e32 v4, 0xffff0000, v146
	v_fmac_f32_e32 v6, v4, v4
	v_lshlrev_b32_e32 v4, 16, v147
	v_fmac_f32_e32 v6, v4, v4
	v_and_b32_e32 v4, 0xffff0000, v147
	v_fmac_f32_e32 v6, v4, v4
	v_lshlrev_b32_e32 v4, 16, v148
	v_fmac_f32_e32 v6, v4, v4
	v_and_b32_e32 v4, 0xffff0000, v148
	v_fmac_f32_e32 v6, v4, v4
	v_lshlrev_b32_e32 v4, 16, v149
	v_fmac_f32_e32 v6, v4, v4
	v_and_b32_e32 v4, 0xffff0000, v149
	v_fmac_f32_e32 v6, v4, v4
	v_lshlrev_b32_e32 v4, 16, v150
	v_fmac_f32_e32 v6, v4, v4
	v_and_b32_e32 v4, 0xffff0000, v150
	v_fmac_f32_e32 v6, v4, v4
	v_lshlrev_b32_e32 v4, 16, v151
	v_fmac_f32_e32 v6, v4, v4
	v_and_b32_e32 v4, 0xffff0000, v151
	v_fmac_f32_e32 v6, v4, v4
	v_and_b32_e32 v5, 0xffff0000, v152
	v_lshlrev_b32_e32 v4, 16, v152
	v_pk_mul_f32 v[4:5], v[4:5], v[4:5]
	s_ashr_i32 s1, s0, 31
	v_add_f32_e32 v4, v4, v6
	v_add_f32_e32 v6, v5, v4
	v_and_b32_e32 v5, 0xffff0000, v153
	v_lshlrev_b32_e32 v4, 16, v153
	v_pk_mul_f32 v[4:5], v[4:5], v[4:5]
	s_lshl_b64 s[0:1], s[0:1], 2
	v_add_f32_e32 v4, v4, v6
	v_add_f32_e32 v6, v5, v4
	v_and_b32_e32 v5, 0xffff0000, v154
	v_lshlrev_b32_e32 v4, 16, v154
	v_pk_mul_f32 v[4:5], v[4:5], v[4:5]
	s_add_u32 s0, s21, s0
	v_add_f32_e32 v4, v4, v6
	v_add_f32_e32 v6, v5, v4
	v_and_b32_e32 v5, 0xffff0000, v155
	v_lshlrev_b32_e32 v4, 16, v155
	v_pk_mul_f32 v[4:5], v[4:5], v[4:5]
	s_addc_u32 s1, s22, s1
	v_add_f32_e32 v4, v4, v6
	s_ashr_i32 s3, s2, 31
	v_add_f32_e32 v4, v5, v4
	global_load_dword v5, v3, s[0:1]
	s_lshl_b64 s[0:1], s[2:3], 2
	s_add_u32 s0, s21, s0
	s_addc_u32 s1, s22, s1
	global_load_dword v7, v3, s[0:1] offset:256
	v_mov_b32_e32 v6, v4
	s_nop 1
	v_permlane32_swap_b32_e32 v4, v6
	s_mov_b32 s0, 0x45fd2000
	v_subrev_u32_e32 v223, s44, v8
	s_barrier
	v_mad_i32_i24 v8, v199, s23, v202
	v_add_u32_e32 v205, v216, v217
	s_mov_b64 s[2:3], exec
	v_lshl_add_u32 v8, s23, 7, v204
	s_waitcnt vmcnt(0)
	v_pk_add_f32 v[4:5], v[4:5], v[6:7]
	s_nop 0
	v_mul_f32_e32 v4, v4, v5
	v_cmp_gt_f32_e32 vcc, s0, v4
	s_nop 1
	s_cmp_eq_u64 vcc, s[2:3]
	s_cbranch_scc1 .Latt_flag_skip
	s_add_i32 s12, s15, 1
	v_mov_b32_e32 v178, 0x27f80
	v_mov_b32_e32 v179, s12
	ds_write_b32 v178, v179
.Latt_flag_skip:
	s_or_b32 s0, s23, 1
	s_sub_i32 s1, s0, s34
	v_lshl_add_u32 v4, s23, v215, v223
	s_min_u32 s0, s0, s1
	v_lshl_add_u32 v12, s0, v215, v223
	v_mad_i32_i24 v18, v199, s0, v202
	s_waitcnt vmcnt(0)
	ds_write_b128 v219, v[116:119]
	ds_write_b64 v220, v[120:121]
	s_nop 0
	ds_write_b128 v219, v[126:129] offset:13312
	s_nop 0
	ds_write_b64 v220, v[130:131] offset:13312
	ds_write_b64 v221, v[122:123] offset:26624
	ds_write_b64 v222, v[124:125] offset:26624
	s_waitcnt lgkmcnt(0)
	s_barrier
	ds_read_b128 v[4:7], v205 offset:6656
	ds_read_b128 v[8:11], v205
	ds_read_b128 v[36:39], v205 offset:32
	ds_read_b128 v[40:43], v205 offset:6688
	s_waitcnt lgkmcnt(2)
	v_mfma_f32_32x32x16_bf16 v[20:35], v[8:11], v[132:135], 0
	v_mfma_f32_32x32x16_bf16 v[4:19], v[4:7], v[132:135], 0
	s_waitcnt lgkmcnt(1)
	v_mfma_f32_32x32x16_bf16 v[20:35], v[36:39], v[136:139], v[20:35]
	s_waitcnt lgkmcnt(0)
	v_mfma_f32_32x32x16_bf16 v[4:19], v[40:43], v[136:139], v[4:19]
	ds_read_b128 v[36:39], v205 offset:64
	ds_read_b128 v[40:43], v205 offset:6720
	s_waitcnt lgkmcnt(1)
	v_mfma_f32_32x32x16_bf16 v[20:35], v[36:39], v[140:143], v[20:35]
	s_waitcnt lgkmcnt(0)
	v_mfma_f32_32x32x16_bf16 v[4:19], v[40:43], v[140:143], v[4:19]
	ds_read_b128 v[36:39], v205 offset:96
	ds_read_b128 v[40:43], v205 offset:6752
	s_waitcnt lgkmcnt(1)
	v_mfma_f32_32x32x16_bf16 v[20:35], v[36:39], v[144:147], v[20:35]
	s_waitcnt lgkmcnt(0)
	v_mfma_f32_32x32x16_bf16 v[4:19], v[40:43], v[144:147], v[4:19]
	ds_read_b128 v[36:39], v205 offset:128
	ds_read_b128 v[40:43], v205 offset:6784
	s_waitcnt lgkmcnt(1)
	v_mfma_f32_32x32x16_bf16 v[20:35], v[36:39], v[148:151], v[20:35]
	s_waitcnt lgkmcnt(0)
	v_mfma_f32_32x32x16_bf16 v[4:19], v[40:43], v[148:151], v[4:19]
	ds_read_b128 v[36:39], v205 offset:160
	ds_read_b128 v[40:43], v205 offset:6816
	s_waitcnt lgkmcnt(0)
	s_barrier
	v_mfma_f32_32x32x16_bf16 v[20:35], v[36:39], v[152:155], v[20:35]
	v_mfma_f32_32x32x16_bf16 v[4:19], v[40:43], v[152:155], v[4:19]
	v_mov_b32_e32 v178, 0x27f80
	ds_read_b32 v179, v178
	s_add_i32 s12, s15, 1
	s_waitcnt lgkmcnt(0)
	v_cmp_ne_u32_e64 s[0:1], s12, v179
	s_nop 1
	s_and_b64 vcc, vcc, s[0:1]
	s_and_saveexec_b64 s[0:1], s[42:43]
	s_setprio 1
	s_or_b64 exec, exec, s[0:1]
	s_cmp_eq_u64 vcc, s[2:3]
	s_mov_b64 s[0:1], -1
	s_cbranch_scc1 .LBB0_1136
	v_mov_b32_e32 v50, v3
	v_mov_b32_e32 v51, v3
	v_mov_b32_e32 v36, v3
	v_mov_b32_e32 v37, v3
	v_mov_b32_e32 v38, v3
	v_mov_b32_e32 v39, v3
	v_mov_b32_e32 v40, v3
	v_mov_b32_e32 v41, v3
	v_mov_b32_e32 v42, v3
	v_mov_b32_e32 v43, v3
	v_mov_b32_e32 v44, v3
	v_mov_b32_e32 v45, v3
	v_mov_b32_e32 v46, v3
	v_mov_b32_e32 v47, v3
	v_mov_b32_e32 v48, v3
	v_mov_b32_e32 v49, v3
	v_mov_b64_e32 v[66:67], v[50:51]
	v_mov_b64_e32 v[82:83], v[34:35]
	v_mov_b64_e32 v[98:99], v[18:19]
	s_mov_b32 s0, 0
	v_mov_b32_e32 v224, 0
	v_mov_b32_e32 v225, 0xf149f2ca
	v_mov_b64_e32 v[64:65], v[48:49]
	v_mov_b64_e32 v[62:63], v[46:47]
	v_mov_b64_e32 v[60:61], v[44:45]
	v_mov_b64_e32 v[58:59], v[42:43]
	v_mov_b64_e32 v[56:57], v[40:41]
	v_mov_b64_e32 v[54:55], v[38:39]
	v_mov_b64_e32 v[52:53], v[36:37]
	v_mov_b64_e32 v[80:81], v[32:33]
	v_mov_b64_e32 v[78:79], v[30:31]
	v_mov_b64_e32 v[76:77], v[28:29]
	v_mov_b64_e32 v[74:75], v[26:27]
	v_mov_b64_e32 v[72:73], v[24:25]
	v_mov_b64_e32 v[70:71], v[22:23]
	v_mov_b64_e32 v[68:69], v[20:21]
	v_mov_b64_e32 v[96:97], v[16:17]
	v_mov_b64_e32 v[94:95], v[14:15]
	v_mov_b64_e32 v[92:93], v[12:13]
	v_mov_b64_e32 v[90:91], v[10:11]
	v_mov_b64_e32 v[88:89], v[8:9]
	v_mov_b64_e32 v[86:87], v[6:7]
	v_mov_b64_e32 v[84:85], v[4:5]
	s_branch .LBB0_1132
